# attention block heads: wait for the staged V and q loads only (counted), not for the previous block's output stores
# baseline (speedup 1.0000x reference)
.LBB0_599:
	s_add_i32 s0, s49, 0xfffffe01
	s_lshr_b32 s0, s0, 6
	s_cmpk_gt_i32 s49, 0x1ff
	s_cselect_b32 s0, s0, 0
	s_ashr_i32 s1, s49, 31
	s_lshr_b32 s1, s1, 26
	s_add_i32 s1, s1, s49
	s_add_i32 s1, s1, 63
	s_ashr_i32 s1, s1, 6
	s_add_i32 s1, s1, 1
	s_cmpk_lt_i32 s49, 0x7c1
	s_cselect_b32 s44, s1, 32
	v_readfirstlane_b32 s47, v254
	s_sub_i32 s48, s44, s0
	s_waitcnt vmcnt(8)
	ds_write_b128 v214, v[106:109]
	s_waitcnt vmcnt(8)
	ds_write_b128 v215, v[110:113]
	s_cmp_gt_i32 s48, 1
	s_cselect_b64 s[28:29], -1, 0
	s_lshl_b32 s50, s0, 6
	s_cmp_lt_i32 s48, 2
	v_lshlrev_b32_e32 v196, 1, v198
	s_cbranch_scc1 .LBB0_601
	s_add_i32 s2, s50, 64
	v_or_b32_e32 v0, s2, v1
	v_mov_b64_e32 v[2:3], s[26:27]
	v_add_u32_e32 v6, s2, v195
	v_mad_u64_u32 v[4:5], s[0:1], v0, s11, v[2:3]
	v_mad_u64_u32 v[2:3], s[0:1], v6, s11, v[2:3]
	v_lshl_add_u64 v[4:5], v[4:5], 0, v[196:197]
	v_lshl_add_u64 v[2:3], v[2:3], 0, v[196:197]
	global_load_dwordx4 v[106:109], v[4:5], off
	global_load_dwordx4 v[110:113], v[2:3], off
	v_mov_b64_e32 v[2:3], s[24:25]
	v_mad_u64_u32 v[4:5], s[0:1], v0, s11, v[2:3]
	v_lshl_add_u64 v[4:5], v[4:5], 0, v[196:197]
	v_mad_u64_u32 v[2:3], s[0:1], v6, s11, v[2:3]
	v_lshl_add_u64 v[2:3], v[2:3], 0, v[196:197]
	global_load_dwordx4 v[98:101], v[4:5], off
	global_load_dwordx4 v[102:105], v[2:3], off

.LBB0_825:
	s_add_i32 s0, s53, 0xfffff801
	s_lshr_b32 s0, s0, 6
	s_cmpk_gt_i32 s53, 0x7ff
	s_cselect_b32 s52, s0, 0
	s_ashr_i32 s0, s53, 31
	s_lshr_b32 s0, s0, 26
	s_add_i32 s0, s0, s53
	s_add_i32 s0, s0, 63
	s_ashr_i32 s0, s0, 6
	s_add_i32 s0, s0, 1
	v_readfirstlane_b32 s50, v254
	s_cmpk_lt_i32 s53, 0x7c1
	s_cselect_b32 s48, s0, 32
	s_lshr_b32 s0, s50, 1
	s_and_b32 s47, s0, 32
	v_or_b32_e32 v203, s47, v194
	v_lshlrev_b32_e32 v2, 4, v203
	global_load_dword v225, v2, s[8:9]
	s_sub_i32 s51, s48, s52
	s_waitcnt vmcnt(9)
	ds_write_b128 v215, v[106:109]
	s_waitcnt vmcnt(9)
	ds_write_b128 v216, v[110:113]
	s_cmp_gt_i32 s51, 1
	s_cselect_b64 s[34:35], -1, 0
	s_lshl_b32 s54, s52, 6
	s_cmp_lt_i32 s51, 2
	v_lshlrev_b32_e32 v196, 1, v0
	s_cbranch_scc1 .LBB0_827
	s_add_i32 s2, s54, 64
	v_or_b32_e32 v6, s2, v195
	v_mov_b64_e32 v[2:3], s[30:31]
	v_add_u32_e32 v7, s2, v213
	v_mad_u64_u32 v[4:5], s[0:1], v6, s13, v[2:3]
	v_mad_u64_u32 v[2:3], s[0:1], v7, s13, v[2:3]
	v_lshl_add_u64 v[4:5], v[4:5], 0, v[196:197]
	v_lshl_add_u64 v[2:3], v[2:3], 0, v[196:197]
	global_load_dwordx4 v[106:109], v[4:5], off
	global_load_dwordx4 v[110:113], v[2:3], off
	v_mov_b64_e32 v[2:3], s[28:29]
	v_mad_u64_u32 v[4:5], s[0:1], v6, s13, v[2:3]
	v_lshl_add_u64 v[4:5], v[4:5], 0, v[196:197]
	v_mad_u64_u32 v[2:3], s[0:1], v7, s13, v[2:3]
	v_lshl_add_u64 v[2:3], v[2:3], 0, v[196:197]
	global_load_dwordx4 v[98:101], v[4:5], off
	global_load_dwordx4 v[102:105], v[2:3], off
